# SwiGLU HID stores (P1/P13) also write-back (sc1 dropped)
# speedup vs baseline: 1.0162x; 1.0033x over previous
; __device__ __forceinline__ unsigned cvt_pk_bf16(float lo, float hi) { unsigned r; asm volatile("v_cvt_pk_bf16_f32 %0, %1, %2" : "=v"(r) : "v"(lo), "v"(hi)); return r; }
; __device__ __forceinline__ int fresh_lane() { int l; asm volatile("v_mbcnt_lo_u32_b32 %0, -1, 0\n\tv_mbcnt_hi_u32_b32 %0, -1, %0" : "=v"(l)); return l; }
; __device__ __forceinline__ void store16_wt(__amdgpu_buffer_rsrc_t rsrc, unsigned byte_off, v4u v) { __builtin_amdgcn_raw_buffer_store_b128(v, rsrc, byte_off, 0, 16); }
;     __device__ __forceinline__ void operator()(AccRef acc, const Unit& u, int wr, int wc, int, int) const {
;         const int ln_ = fresh_lane(), fr = ln_ & 15, fq = ln_ >> 4;
;         const int row0 = u.pm * 256 + wr * 64 + fr, col0 = u.pn * 128 + wc * 32 + 8 * fq;
;         const __amdgpu_buffer_rsrc_t rsrc = __builtin_amdgcn_make_buffer_rsrc((void*)H, 0, (int)((size_t)M * DFF * 2), 0x00020000);
;         float rs[8]; rows_rstd(ss, row0, fq, ln_, rs);
; #pragma unroll
;         for (int ai = 0; ai < 2; ++ai)
; #pragma unroll
;             for (int m = 0; m < 4; ++m) {
;                 const int row = row0 + ai * 128 + m * 16;
;                 const float r = rs[ai * 4 + m];
;                 float h[8];
; #pragma unroll
;                 for (int n = 0; n < 2; ++n)
; #pragma unroll
;                     for (int j = 0; j < 4; ++j) { const float a = acc[ai][0][m][n][j] * r, b = acc[ai][1][m][n][j] * r; h[4 * n + j] = a * __builtin_amdgcn_rcpf(1.0f + __expf(-a)) * b; }
;                 v4u w; w.x = cvt_pk_bf16(h[0], h[1]); w.y = cvt_pk_bf16(h[2], h[3]); w.z = cvt_pk_bf16(h[4], h[5]); w.w = cvt_pk_bf16(h[6], h[7]);
;                 store16_wt(rsrc, (unsigned)(((size_t)row * DFF + col0) * 2), w);
;             }
.LBB0_138:
	s_lshl_b32 s98, s6, 8
	v_mbcnt_lo_u32_b32 v130, -1, 0
	v_mbcnt_hi_u32_b32 v130, -1, v130
	s_add_i32 s98, s98, s37
	s_lshl_b32 s99, s7, 7
	s_or_b32 s99, s99, s39
	v_and_or_b32 v131, v130, 15, s98
	v_lshrrev_b32_e32 v132, 4, v130
	v_lshl_add_u32 v132, v132, 3, s99
	s_movk_i32 s98, 0x1580
	v_mul_lo_u32 v131, v131, s98
	v_readlane_b32 s20, v254, 15
	v_readlane_b32 s21, v254, 16
	v_readlane_b32 s22, v254, 17
	v_readlane_b32 s23, v254, 18
	v_add_lshl_u32 v131, v132, v131, 1
	v_mul_f32_e32 v126, v242, v126
	v_mul_f32_e32 v127, v242, v127
	v_mul_f32_e32 v128, v242, v128
	v_mul_f32_e32 v129, v242, v129
	v_mul_f32_e32 v118, v242, v118
	v_mul_f32_e32 v119, v242, v119
	v_mul_f32_e32 v120, v242, v120
	v_mul_f32_e32 v121, v242, v121
	v_mul_f32_e32 v122, v242, v122
	v_mul_f32_e32 v123, v242, v123
	v_mul_f32_e32 v124, v242, v124
	v_mul_f32_e32 v125, v242, v125
	v_mul_f32_e32 v114, v242, v114
	v_mul_f32_e32 v115, v242, v115
	v_mul_f32_e32 v116, v242, v116
	v_mul_f32_e32 v117, v242, v117
	v_mul_f32_e32 v140, 0xbfb8aa3b, v126
	v_mul_f32_e32 v141, 0xbfb8aa3b, v127
	v_mul_f32_e32 v142, 0xbfb8aa3b, v128
	v_mul_f32_e32 v143, 0xbfb8aa3b, v129
	v_mul_f32_e32 v144, 0xbfb8aa3b, v118
	v_mul_f32_e32 v145, 0xbfb8aa3b, v119
	v_mul_f32_e32 v146, 0xbfb8aa3b, v120
	v_mul_f32_e32 v147, 0xbfb8aa3b, v121
	v_exp_f32_e32 v140, v140
	v_exp_f32_e32 v141, v141
	v_exp_f32_e32 v142, v142
	v_exp_f32_e32 v143, v143
	v_exp_f32_e32 v144, v144
	v_exp_f32_e32 v145, v145
	v_exp_f32_e32 v146, v146
	v_exp_f32_e32 v147, v147
	v_add_f32_e32 v140, 1.0, v140
	v_add_f32_e32 v141, 1.0, v141
	v_add_f32_e32 v142, 1.0, v142
	v_add_f32_e32 v143, 1.0, v143
	v_add_f32_e32 v144, 1.0, v144
	v_add_f32_e32 v145, 1.0, v145
	v_add_f32_e32 v146, 1.0, v146
	v_add_f32_e32 v147, 1.0, v147
	v_rcp_f32_e32 v140, v140
	v_rcp_f32_e32 v141, v141
	v_rcp_f32_e32 v142, v142
	v_rcp_f32_e32 v143, v143
	v_rcp_f32_e32 v144, v144
	v_rcp_f32_e32 v145, v145
	v_rcp_f32_e32 v146, v146
	v_rcp_f32_e32 v147, v147
	v_mul_f32_e32 v126, v126, v140
	v_mul_f32_e32 v127, v127, v141
	v_mul_f32_e32 v128, v128, v142
	v_mul_f32_e32 v129, v129, v143
	v_mul_f32_e32 v118, v118, v144
	v_mul_f32_e32 v119, v119, v145
	v_mul_f32_e32 v120, v120, v146
	v_mul_f32_e32 v121, v121, v147
	v_mul_f32_e32 v126, v122, v126
	v_mul_f32_e32 v127, v123, v127
	v_mul_f32_e32 v128, v124, v128
	v_mul_f32_e32 v129, v125, v129
	v_mul_f32_e32 v118, v114, v118
	v_mul_f32_e32 v119, v115, v119
	v_mul_f32_e32 v120, v116, v120
	v_mul_f32_e32 v121, v117, v121
	v_cvt_pk_bf16_f32 v148, v126, v127
	v_cvt_pk_bf16_f32 v149, v128, v129
	v_cvt_pk_bf16_f32 v150, v118, v119
	v_cvt_pk_bf16_f32 v151, v120, v121
	v_mov_b32_e32 v133, v131
	buffer_store_dwordx4 v[148:151], v133, s[20:23], 0 offen
	v_mul_f32_e32 v110, v243, v110
	v_mul_f32_e32 v111, v243, v111
	v_mul_f32_e32 v112, v243, v112
	v_mul_f32_e32 v113, v243, v113
	v_mul_f32_e32 v102, v243, v102
	v_mul_f32_e32 v103, v243, v103
	v_mul_f32_e32 v104, v243, v104
	v_mul_f32_e32 v105, v243, v105
	v_mul_f32_e32 v106, v243, v106
	v_mul_f32_e32 v107, v243, v107
	v_mul_f32_e32 v108, v243, v108
	v_mul_f32_e32 v109, v243, v109
	v_mul_f32_e32 v98, v243, v98
	v_mul_f32_e32 v99, v243, v99
	v_mul_f32_e32 v100, v243, v100
	v_mul_f32_e32 v101, v243, v101
	v_mul_f32_e32 v140, 0xbfb8aa3b, v110
	v_mul_f32_e32 v141, 0xbfb8aa3b, v111
	v_mul_f32_e32 v142, 0xbfb8aa3b, v112
	v_mul_f32_e32 v143, 0xbfb8aa3b, v113
	v_mul_f32_e32 v144, 0xbfb8aa3b, v102
	v_mul_f32_e32 v145, 0xbfb8aa3b, v103
	v_mul_f32_e32 v146, 0xbfb8aa3b, v104
	v_mul_f32_e32 v147, 0xbfb8aa3b, v105
	v_exp_f32_e32 v140, v140
	v_exp_f32_e32 v141, v141
	v_exp_f32_e32 v142, v142
	v_exp_f32_e32 v143, v143
	v_exp_f32_e32 v144, v144
	v_exp_f32_e32 v145, v145
	v_exp_f32_e32 v146, v146
	v_exp_f32_e32 v147, v147
	v_add_f32_e32 v140, 1.0, v140
	v_add_f32_e32 v141, 1.0, v141
	v_add_f32_e32 v142, 1.0, v142
	v_add_f32_e32 v143, 1.0, v143
	v_add_f32_e32 v144, 1.0, v144
	v_add_f32_e32 v145, 1.0, v145
	v_add_f32_e32 v146, 1.0, v146
	v_add_f32_e32 v147, 1.0, v147
	v_rcp_f32_e32 v140, v140
	v_rcp_f32_e32 v141, v141
	v_rcp_f32_e32 v142, v142
	v_rcp_f32_e32 v143, v143
	v_rcp_f32_e32 v144, v144
	v_rcp_f32_e32 v145, v145
	v_rcp_f32_e32 v146, v146
	v_rcp_f32_e32 v147, v147
	v_mul_f32_e32 v110, v110, v140
	v_mul_f32_e32 v111, v111, v141
	v_mul_f32_e32 v112, v112, v142
	v_mul_f32_e32 v113, v113, v143
	v_mul_f32_e32 v102, v102, v144
	v_mul_f32_e32 v103, v103, v145
	v_mul_f32_e32 v104, v104, v146
	v_mul_f32_e32 v105, v105, v147
	v_mul_f32_e32 v110, v106, v110
	v_mul_f32_e32 v111, v107, v111
	v_mul_f32_e32 v112, v108, v112
	v_mul_f32_e32 v113, v109, v113
	v_mul_f32_e32 v102, v98, v102
	v_mul_f32_e32 v103, v99, v103
	v_mul_f32_e32 v104, v100, v104
	v_mul_f32_e32 v105, v101, v105
	v_cvt_pk_bf16_f32 v152, v110, v111
	v_cvt_pk_bf16_f32 v153, v112, v113
	v_cvt_pk_bf16_f32 v154, v102, v103
	v_cvt_pk_bf16_f32 v155, v104, v105
	v_add_u32_e32 v133, 0x2b000, v131
	buffer_store_dwordx4 v[152:155], v133, s[20:23], 0 offen
	v_mul_f32_e32 v94, v244, v94
	v_mul_f32_e32 v95, v244, v95
	v_mul_f32_e32 v96, v244, v96
	v_mul_f32_e32 v97, v244, v97
	v_mul_f32_e32 v86, v244, v86
	v_mul_f32_e32 v87, v244, v87
	v_mul_f32_e32 v88, v244, v88
	v_mul_f32_e32 v89, v244, v89
	v_mul_f32_e32 v90, v244, v90
	v_mul_f32_e32 v91, v244, v91
	v_mul_f32_e32 v92, v244, v92
	v_mul_f32_e32 v93, v244, v93
	v_mul_f32_e32 v82, v244, v82
	v_mul_f32_e32 v83, v244, v83
	v_mul_f32_e32 v84, v244, v84
	v_mul_f32_e32 v85, v244, v85
	v_mul_f32_e32 v140, 0xbfb8aa3b, v94
	v_mul_f32_e32 v141, 0xbfb8aa3b, v95
	v_mul_f32_e32 v142, 0xbfb8aa3b, v96
	v_mul_f32_e32 v143, 0xbfb8aa3b, v97
	v_mul_f32_e32 v144, 0xbfb8aa3b, v86
	v_mul_f32_e32 v145, 0xbfb8aa3b, v87
; __device__ __forceinline__ unsigned cvt_pk_bf16(float lo, float hi) { unsigned r; asm volatile("v_cvt_pk_bf16_f32 %0, %1, %2" : "=v"(r) : "v"(lo), "v"(hi)); return r; }
; __device__ __forceinline__ void store16_wt(__amdgpu_buffer_rsrc_t rsrc, unsigned byte_off, v4u v) { __builtin_amdgcn_raw_buffer_store_b128(v, rsrc, byte_off, 0, 16); }
;     __device__ __forceinline__ void operator()(AccRef acc, const Unit& u, int wr, int wc, int, int) const {
;     ...
; #pragma unroll
;         for (int ai = 0; ai < 2; ++ai)
; #pragma unroll
;             for (int m = 0; m < 4; ++m) {
;                 const int row = row0 + ai * 128 + m * 16;
;                 const float r = rs[ai * 4 + m];
;                 float h[8];
; #pragma unroll
;                 for (int n = 0; n < 2; ++n)
; #pragma unroll
;                     for (int j = 0; j < 4; ++j) { const float a = acc[ai][0][m][n][j] * r, b = acc[ai][1][m][n][j] * r; h[4 * n + j] = a * __builtin_amdgcn_rcpf(1.0f + __expf(-a)) * b; }
;                 v4u w; w.x = cvt_pk_bf16(h[0], h[1]); w.y = cvt_pk_bf16(h[2], h[3]); w.z = cvt_pk_bf16(h[4], h[5]); w.w = cvt_pk_bf16(h[6], h[7]);
;                 store16_wt(rsrc, (unsigned)(((size_t)row * DFF + col0) * 2), w);
;             }
	v_mul_f32_e32 v146, 0xbfb8aa3b, v88
	v_mul_f32_e32 v147, 0xbfb8aa3b, v89
	v_exp_f32_e32 v140, v140
	v_exp_f32_e32 v141, v141
	v_exp_f32_e32 v142, v142
	v_exp_f32_e32 v143, v143
	v_exp_f32_e32 v144, v144
	v_exp_f32_e32 v145, v145
	v_exp_f32_e32 v146, v146
	v_exp_f32_e32 v147, v147
	v_add_f32_e32 v140, 1.0, v140
	v_add_f32_e32 v141, 1.0, v141
	v_add_f32_e32 v142, 1.0, v142
	v_add_f32_e32 v143, 1.0, v143
	v_add_f32_e32 v144, 1.0, v144
	v_add_f32_e32 v145, 1.0, v145
	v_add_f32_e32 v146, 1.0, v146
	v_add_f32_e32 v147, 1.0, v147
	v_rcp_f32_e32 v140, v140
	v_rcp_f32_e32 v141, v141
	v_rcp_f32_e32 v142, v142
	v_rcp_f32_e32 v143, v143
	v_rcp_f32_e32 v144, v144
	v_rcp_f32_e32 v145, v145
	v_rcp_f32_e32 v146, v146
	v_rcp_f32_e32 v147, v147
	v_mul_f32_e32 v94, v94, v140
	v_mul_f32_e32 v95, v95, v141
	v_mul_f32_e32 v96, v96, v142
	v_mul_f32_e32 v97, v97, v143
	v_mul_f32_e32 v86, v86, v144
	v_mul_f32_e32 v87, v87, v145
	v_mul_f32_e32 v88, v88, v146
	v_mul_f32_e32 v89, v89, v147
	v_mul_f32_e32 v94, v90, v94
	v_mul_f32_e32 v95, v91, v95
	v_mul_f32_e32 v96, v92, v96
	v_mul_f32_e32 v97, v93, v97
	v_mul_f32_e32 v86, v82, v86
	v_mul_f32_e32 v87, v83, v87
	v_mul_f32_e32 v88, v84, v88
	v_mul_f32_e32 v89, v85, v89
	v_cvt_pk_bf16_f32 v148, v94, v95
	v_cvt_pk_bf16_f32 v149, v96, v97
	v_cvt_pk_bf16_f32 v150, v86, v87
	v_cvt_pk_bf16_f32 v151, v88, v89
	v_add_u32_e32 v133, 0x56000, v131
	buffer_store_dwordx4 v[148:151], v133, s[20:23], 0 offen
	v_mul_f32_e32 v78, v245, v78
	v_mul_f32_e32 v79, v245, v79
	v_mul_f32_e32 v80, v245, v80
	v_mul_f32_e32 v81, v245, v81
	v_mul_f32_e32 v70, v245, v70
	v_mul_f32_e32 v71, v245, v71
	v_mul_f32_e32 v72, v245, v72
	v_mul_f32_e32 v73, v245, v73
	v_mul_f32_e32 v74, v245, v74
	v_mul_f32_e32 v75, v245, v75
	v_mul_f32_e32 v76, v245, v76
	v_mul_f32_e32 v77, v245, v77
	v_mul_f32_e32 v66, v245, v66
	v_mul_f32_e32 v67, v245, v67
	v_mul_f32_e32 v68, v245, v68
	v_mul_f32_e32 v69, v245, v69
	v_mul_f32_e32 v140, 0xbfb8aa3b, v78
	v_mul_f32_e32 v141, 0xbfb8aa3b, v79
	v_mul_f32_e32 v142, 0xbfb8aa3b, v80
	v_mul_f32_e32 v143, 0xbfb8aa3b, v81
	v_mul_f32_e32 v144, 0xbfb8aa3b, v70
	v_mul_f32_e32 v145, 0xbfb8aa3b, v71
	v_mul_f32_e32 v146, 0xbfb8aa3b, v72
	v_mul_f32_e32 v147, 0xbfb8aa3b, v73
	v_exp_f32_e32 v140, v140
	v_exp_f32_e32 v141, v141
	v_exp_f32_e32 v142, v142
	v_exp_f32_e32 v143, v143
	v_exp_f32_e32 v144, v144
	v_exp_f32_e32 v145, v145
	v_exp_f32_e32 v146, v146
	v_exp_f32_e32 v147, v147
	v_add_f32_e32 v140, 1.0, v140
	v_add_f32_e32 v141, 1.0, v141
	v_add_f32_e32 v142, 1.0, v142
	v_add_f32_e32 v143, 1.0, v143
	v_add_f32_e32 v144, 1.0, v144
	v_add_f32_e32 v145, 1.0, v145
	v_add_f32_e32 v146, 1.0, v146
	v_add_f32_e32 v147, 1.0, v147
	v_rcp_f32_e32 v140, v140
	v_rcp_f32_e32 v141, v141
	v_rcp_f32_e32 v142, v142
	v_rcp_f32_e32 v143, v143
	v_rcp_f32_e32 v144, v144
	v_rcp_f32_e32 v145, v145
	v_rcp_f32_e32 v146, v146
	v_rcp_f32_e32 v147, v147
	v_mul_f32_e32 v78, v78, v140
	v_mul_f32_e32 v79, v79, v141
	v_mul_f32_e32 v80, v80, v142
	v_mul_f32_e32 v81, v81, v143
	v_mul_f32_e32 v70, v70, v144
	v_mul_f32_e32 v71, v71, v145
	v_mul_f32_e32 v72, v72, v146
	v_mul_f32_e32 v73, v73, v147
	v_mul_f32_e32 v78, v74, v78
	v_mul_f32_e32 v79, v75, v79
	v_mul_f32_e32 v80, v76, v80
	v_mul_f32_e32 v81, v77, v81
	v_mul_f32_e32 v70, v66, v70
	v_mul_f32_e32 v71, v67, v71
	v_mul_f32_e32 v72, v68, v72
	v_mul_f32_e32 v73, v69, v73
	v_cvt_pk_bf16_f32 v152, v78, v79
	v_cvt_pk_bf16_f32 v153, v80, v81
	v_cvt_pk_bf16_f32 v154, v70, v71
	v_cvt_pk_bf16_f32 v155, v72, v73
	v_add_u32_e32 v133, 0x81000, v131
	buffer_store_dwordx4 v[152:155], v133, s[20:23], 0 offen
	v_mul_f32_e32 v62, v246, v62
	v_mul_f32_e32 v63, v246, v63
	v_mul_f32_e32 v64, v246, v64
	v_mul_f32_e32 v65, v246, v65
	v_mul_f32_e32 v54, v246, v54
	v_mul_f32_e32 v55, v246, v55
	v_mul_f32_e32 v56, v246, v56
	v_mul_f32_e32 v57, v246, v57
	v_mul_f32_e32 v58, v246, v58
	v_mul_f32_e32 v59, v246, v59
	v_mul_f32_e32 v60, v246, v60
	v_mul_f32_e32 v61, v246, v61
	v_mul_f32_e32 v50, v246, v50
	v_mul_f32_e32 v51, v246, v51
	v_mul_f32_e32 v52, v246, v52
	v_mul_f32_e32 v53, v246, v53
	v_mul_f32_e32 v140, 0xbfb8aa3b, v62
	v_mul_f32_e32 v141, 0xbfb8aa3b, v63
	v_mul_f32_e32 v142, 0xbfb8aa3b, v64
	v_mul_f32_e32 v143, 0xbfb8aa3b, v65
	v_mul_f32_e32 v144, 0xbfb8aa3b, v54
	v_mul_f32_e32 v145, 0xbfb8aa3b, v55
	v_mul_f32_e32 v146, 0xbfb8aa3b, v56
	v_mul_f32_e32 v147, 0xbfb8aa3b, v57
	v_exp_f32_e32 v140, v140
	v_exp_f32_e32 v141, v141
	v_exp_f32_e32 v142, v142
	v_exp_f32_e32 v143, v143
	v_exp_f32_e32 v144, v144
	v_exp_f32_e32 v145, v145
	v_exp_f32_e32 v146, v146
	v_exp_f32_e32 v147, v147
	v_add_f32_e32 v140, 1.0, v140
	v_add_f32_e32 v141, 1.0, v141
	v_add_f32_e32 v142, 1.0, v142
	v_add_f32_e32 v143, 1.0, v143
	v_add_f32_e32 v144, 1.0, v144
	v_add_f32_e32 v145, 1.0, v145
	v_add_f32_e32 v146, 1.0, v146
	v_add_f32_e32 v147, 1.0, v147
	v_rcp_f32_e32 v140, v140
	v_rcp_f32_e32 v141, v141
	v_rcp_f32_e32 v142, v142
	v_rcp_f32_e32 v143, v143
	v_rcp_f32_e32 v144, v144
	v_rcp_f32_e32 v145, v145
	v_rcp_f32_e32 v146, v146
	v_rcp_f32_e32 v147, v147
	v_mul_f32_e32 v62, v62, v140
	v_mul_f32_e32 v63, v63, v141
	v_mul_f32_e32 v64, v64, v142
	v_mul_f32_e32 v65, v65, v143
	v_mul_f32_e32 v54, v54, v144
	v_mul_f32_e32 v55, v55, v145
	v_mul_f32_e32 v56, v56, v146
	v_mul_f32_e32 v57, v57, v147
	v_mul_f32_e32 v62, v58, v62
	v_mul_f32_e32 v63, v59, v63
	v_mul_f32_e32 v64, v60, v64
	v_mul_f32_e32 v65, v61, v65
	v_mul_f32_e32 v54, v50, v54
	v_mul_f32_e32 v55, v51, v55
	v_mul_f32_e32 v56, v52, v56
	v_mul_f32_e32 v57, v53, v57
	v_cvt_pk_bf16_f32 v148, v62, v63
	v_cvt_pk_bf16_f32 v149, v64, v65
	v_cvt_pk_bf16_f32 v150, v54, v55
	v_cvt_pk_bf16_f32 v151, v56, v57
; __device__ __forceinline__ unsigned cvt_pk_bf16(float lo, float hi) { unsigned r; asm volatile("v_cvt_pk_bf16_f32 %0, %1, %2" : "=v"(r) : "v"(lo), "v"(hi)); return r; }
; __device__ __forceinline__ void store16_wt(__amdgpu_buffer_rsrc_t rsrc, unsigned byte_off, v4u v) { __builtin_amdgcn_raw_buffer_store_b128(v, rsrc, byte_off, 0, 16); }
;     __device__ __forceinline__ void operator()(AccRef acc, const Unit& u, int wr, int wc, int, int) const {
;     ...
; #pragma unroll
;         for (int ai = 0; ai < 2; ++ai)
; #pragma unroll
;             for (int m = 0; m < 4; ++m) {
;                 const int row = row0 + ai * 128 + m * 16;
;                 const float r = rs[ai * 4 + m];
;                 float h[8];
; #pragma unroll
;                 for (int n = 0; n < 2; ++n)
; #pragma unroll
;                     for (int j = 0; j < 4; ++j) { const float a = acc[ai][0][m][n][j] * r, b = acc[ai][1][m][n][j] * r; h[4 * n + j] = a * __builtin_amdgcn_rcpf(1.0f + __expf(-a)) * b; }
;                 v4u w; w.x = cvt_pk_bf16(h[0], h[1]); w.y = cvt_pk_bf16(h[2], h[3]); w.z = cvt_pk_bf16(h[4], h[5]); w.w = cvt_pk_bf16(h[6], h[7]);
;                 store16_wt(rsrc, (unsigned)(((size_t)row * DFF + col0) * 2), w);
;             }
	v_add_u32_e32 v133, 0x158000, v131
	buffer_store_dwordx4 v[148:151], v133, s[20:23], 0 offen
	v_mul_f32_e32 v46, v247, v46
	v_mul_f32_e32 v47, v247, v47
	v_mul_f32_e32 v48, v247, v48
	v_mul_f32_e32 v49, v247, v49
	v_mul_f32_e32 v38, v247, v38
	v_mul_f32_e32 v39, v247, v39
	v_mul_f32_e32 v40, v247, v40
	v_mul_f32_e32 v41, v247, v41
	v_mul_f32_e32 v42, v247, v42
	v_mul_f32_e32 v43, v247, v43
	v_mul_f32_e32 v44, v247, v44
	v_mul_f32_e32 v45, v247, v45
	v_mul_f32_e32 v34, v247, v34
	v_mul_f32_e32 v35, v247, v35
	v_mul_f32_e32 v36, v247, v36
	v_mul_f32_e32 v37, v247, v37
	v_mul_f32_e32 v140, 0xbfb8aa3b, v46
	v_mul_f32_e32 v141, 0xbfb8aa3b, v47
	v_mul_f32_e32 v142, 0xbfb8aa3b, v48
	v_mul_f32_e32 v143, 0xbfb8aa3b, v49
	v_mul_f32_e32 v144, 0xbfb8aa3b, v38
	v_mul_f32_e32 v145, 0xbfb8aa3b, v39
	v_mul_f32_e32 v146, 0xbfb8aa3b, v40
	v_mul_f32_e32 v147, 0xbfb8aa3b, v41
	v_exp_f32_e32 v140, v140
	v_exp_f32_e32 v141, v141
	v_exp_f32_e32 v142, v142
	v_exp_f32_e32 v143, v143
	v_exp_f32_e32 v144, v144
	v_exp_f32_e32 v145, v145
	v_exp_f32_e32 v146, v146
	v_exp_f32_e32 v147, v147
	v_add_f32_e32 v140, 1.0, v140
	v_add_f32_e32 v141, 1.0, v141
	v_add_f32_e32 v142, 1.0, v142
	v_add_f32_e32 v143, 1.0, v143
	v_add_f32_e32 v144, 1.0, v144
	v_add_f32_e32 v145, 1.0, v145
	v_add_f32_e32 v146, 1.0, v146
	v_add_f32_e32 v147, 1.0, v147
	v_rcp_f32_e32 v140, v140
	v_rcp_f32_e32 v141, v141
	v_rcp_f32_e32 v142, v142
	v_rcp_f32_e32 v143, v143
	v_rcp_f32_e32 v144, v144
	v_rcp_f32_e32 v145, v145
	v_rcp_f32_e32 v146, v146
	v_rcp_f32_e32 v147, v147
	v_mul_f32_e32 v46, v46, v140
	v_mul_f32_e32 v47, v47, v141
	v_mul_f32_e32 v48, v48, v142
	v_mul_f32_e32 v49, v49, v143
	v_mul_f32_e32 v38, v38, v144
	v_mul_f32_e32 v39, v39, v145
	v_mul_f32_e32 v40, v40, v146
	v_mul_f32_e32 v41, v41, v147
	v_mul_f32_e32 v46, v42, v46
	v_mul_f32_e32 v47, v43, v47
	v_mul_f32_e32 v48, v44, v48
	v_mul_f32_e32 v49, v45, v49
	v_mul_f32_e32 v38, v34, v38
	v_mul_f32_e32 v39, v35, v39
	v_mul_f32_e32 v40, v36, v40
	v_mul_f32_e32 v41, v37, v41
	v_cvt_pk_bf16_f32 v152, v46, v47
	v_cvt_pk_bf16_f32 v153, v48, v49
	v_cvt_pk_bf16_f32 v154, v38, v39
	v_cvt_pk_bf16_f32 v155, v40, v41
	v_add_u32_e32 v133, 0x183000, v131
	buffer_store_dwordx4 v[152:155], v133, s[20:23], 0 offen
	v_mul_f32_e32 v30, v248, v30
	v_mul_f32_e32 v31, v248, v31
	v_mul_f32_e32 v32, v248, v32
	v_mul_f32_e32 v33, v248, v33
	v_mul_f32_e32 v22, v248, v22
	v_mul_f32_e32 v23, v248, v23
	v_mul_f32_e32 v24, v248, v24
	v_mul_f32_e32 v25, v248, v25
	v_mul_f32_e32 v26, v248, v26
	v_mul_f32_e32 v27, v248, v27
	v_mul_f32_e32 v28, v248, v28
	v_mul_f32_e32 v29, v248, v29
	v_mul_f32_e32 v18, v248, v18
	v_mul_f32_e32 v19, v248, v19
	v_mul_f32_e32 v20, v248, v20
	v_mul_f32_e32 v21, v248, v21
	v_mul_f32_e32 v140, 0xbfb8aa3b, v30
	v_mul_f32_e32 v141, 0xbfb8aa3b, v31
	v_mul_f32_e32 v142, 0xbfb8aa3b, v32
	v_mul_f32_e32 v143, 0xbfb8aa3b, v33
	v_mul_f32_e32 v144, 0xbfb8aa3b, v22
	v_mul_f32_e32 v145, 0xbfb8aa3b, v23
	v_mul_f32_e32 v146, 0xbfb8aa3b, v24
	v_mul_f32_e32 v147, 0xbfb8aa3b, v25
	v_exp_f32_e32 v140, v140
	v_exp_f32_e32 v141, v141
	v_exp_f32_e32 v142, v142
	v_exp_f32_e32 v143, v143
	v_exp_f32_e32 v144, v144
	v_exp_f32_e32 v145, v145
	v_exp_f32_e32 v146, v146
	v_exp_f32_e32 v147, v147
	v_add_f32_e32 v140, 1.0, v140
	v_add_f32_e32 v141, 1.0, v141
	v_add_f32_e32 v142, 1.0, v142
	v_add_f32_e32 v143, 1.0, v143
	v_add_f32_e32 v144, 1.0, v144
	v_add_f32_e32 v145, 1.0, v145
	v_add_f32_e32 v146, 1.0, v146
	v_add_f32_e32 v147, 1.0, v147
	v_rcp_f32_e32 v140, v140
	v_rcp_f32_e32 v141, v141
	v_rcp_f32_e32 v142, v142
	v_rcp_f32_e32 v143, v143
	v_rcp_f32_e32 v144, v144
	v_rcp_f32_e32 v145, v145
	v_rcp_f32_e32 v146, v146
	v_rcp_f32_e32 v147, v147
	v_mul_f32_e32 v30, v30, v140
	v_mul_f32_e32 v31, v31, v141
	v_mul_f32_e32 v32, v32, v142
	v_mul_f32_e32 v33, v33, v143
	v_mul_f32_e32 v22, v22, v144
	v_mul_f32_e32 v23, v23, v145
	v_mul_f32_e32 v24, v24, v146
	v_mul_f32_e32 v25, v25, v147
	v_mul_f32_e32 v30, v26, v30
	v_mul_f32_e32 v31, v27, v31
	v_mul_f32_e32 v32, v28, v32
	v_mul_f32_e32 v33, v29, v33
	v_mul_f32_e32 v22, v18, v22
	v_mul_f32_e32 v23, v19, v23
	v_mul_f32_e32 v24, v20, v24
	v_mul_f32_e32 v25, v21, v25
	v_cvt_pk_bf16_f32 v148, v30, v31
	v_cvt_pk_bf16_f32 v149, v32, v33
	v_cvt_pk_bf16_f32 v150, v22, v23
	v_cvt_pk_bf16_f32 v151, v24, v25
	v_add_u32_e32 v133, 0x1ae000, v131
	buffer_store_dwordx4 v[148:151], v133, s[20:23], 0 offen
	v_mul_f32_e32 v14, v249, v14
	v_mul_f32_e32 v15, v249, v15
	v_mul_f32_e32 v16, v249, v16
	v_mul_f32_e32 v17, v249, v17
	v_mul_f32_e32 v4, v249, v4
	v_mul_f32_e32 v5, v249, v5
	v_mul_f32_e32 v6, v249, v6
	v_mul_f32_e32 v7, v249, v7
	v_mul_f32_e32 v10, v249, v10
	v_mul_f32_e32 v11, v249, v11
	v_mul_f32_e32 v12, v249, v12
	v_mul_f32_e32 v13, v249, v13
	v_mul_f32_e32 v0, v249, v0
	v_mul_f32_e32 v1, v249, v1
	v_mul_f32_e32 v2, v249, v2
	v_mul_f32_e32 v3, v249, v3
	v_mul_f32_e32 v140, 0xbfb8aa3b, v14
	v_mul_f32_e32 v141, 0xbfb8aa3b, v15
	v_mul_f32_e32 v142, 0xbfb8aa3b, v16
	v_mul_f32_e32 v143, 0xbfb8aa3b, v17
	v_mul_f32_e32 v144, 0xbfb8aa3b, v4
	v_mul_f32_e32 v145, 0xbfb8aa3b, v5
	v_mul_f32_e32 v146, 0xbfb8aa3b, v6
	v_mul_f32_e32 v147, 0xbfb8aa3b, v7
	v_exp_f32_e32 v140, v140
	v_exp_f32_e32 v141, v141
	v_exp_f32_e32 v142, v142
	v_exp_f32_e32 v143, v143
	v_exp_f32_e32 v144, v144
	v_exp_f32_e32 v145, v145
	v_exp_f32_e32 v146, v146
	v_exp_f32_e32 v147, v147
	v_add_f32_e32 v140, 1.0, v140
	v_add_f32_e32 v141, 1.0, v141
	v_add_f32_e32 v142, 1.0, v142
	v_add_f32_e32 v143, 1.0, v143
	v_add_f32_e32 v144, 1.0, v144
	v_add_f32_e32 v145, 1.0, v145
	v_add_f32_e32 v146, 1.0, v146
	v_add_f32_e32 v147, 1.0, v147
	v_rcp_f32_e32 v140, v140
	v_rcp_f32_e32 v141, v141
	v_rcp_f32_e32 v142, v142
	v_rcp_f32_e32 v143, v143
	v_rcp_f32_e32 v144, v144
	v_rcp_f32_e32 v145, v145
	v_rcp_f32_e32 v146, v146
	v_rcp_f32_e32 v147, v147
	v_mul_f32_e32 v14, v14, v140
	v_mul_f32_e32 v15, v15, v141
	v_mul_f32_e32 v16, v16, v142
	v_mul_f32_e32 v17, v17, v143
	v_mul_f32_e32 v4, v4, v144
	v_mul_f32_e32 v5, v5, v145
	v_mul_f32_e32 v6, v6, v146
	v_mul_f32_e32 v7, v7, v147
	v_mul_f32_e32 v14, v10, v14
	v_mul_f32_e32 v15, v11, v15
	v_mul_f32_e32 v16, v12, v16
	v_mul_f32_e32 v17, v13, v17
	v_mul_f32_e32 v4, v0, v4
	v_mul_f32_e32 v5, v1, v5
	v_mul_f32_e32 v6, v2, v6
	v_mul_f32_e32 v7, v3, v7
	v_cvt_pk_bf16_f32 v152, v14, v15
	v_cvt_pk_bf16_f32 v153, v16, v17
	v_cvt_pk_bf16_f32 v154, v4, v5
	v_cvt_pk_bf16_f32 v155, v6, v7
	v_add_u32_e32 v133, 0x1d9000, v131
	buffer_store_dwordx4 v[152:155], v133, s[20:23], 0 offen
	s_mov_b64 s[6:7], -1
	s_andn2_b64 vcc, exec, s[4:5]
	s_cbranch_vccnz .LBB0_131
	s_andn2_b64 vcc, exec, s[0:1]
	s_cbranch_vccnz .LBB0_130
	s_barrier
	s_branch .LBB0_130
